# gates (y*silu(z) + rmsnorm): the paired 6-hop ds_bpermute wave sums replaced by DPP row operations + v_permlane16/32_swap
# speedup vs baseline: 1.0452x; 1.0001x over previous
; __device__ __forceinline__ float silu_f(float x) { return x * __builtin_amdgcn_rcpf(1.f + __expf(-x)); }
; __device__ __forceinline__ f32x4 bf4(const uint2 u) { return (f32x4){__uint_as_float(u.x << 16), __uint_as_float(u.x & 0xffff0000u), __uint_as_float(u.y << 16), __uint_as_float(u.y & 0xffff0000u)}; }
;     template <class T> __device__ __forceinline__ T* w(size_t off) const { return (T*)(p->ws + off); }
; __device__ __forceinline__ void ph_gates(const Ctx& c, int layer, int tile) {
;     const int lane = c.tid & 63, n0 = tile * 32 + (c.tid >> 6) * 8, t4 = lane * 4;
;     const float dsk = c.in(26)[layer * 4 + (lane >> 4)];
;     const f32x4 gn = *(const f32x4*)(c.in(27) + layer * 256 + t4);
;     f32x4 ys[8]; uint2 xr[8], zr[8];
; #pragma unroll
;     for (int u = 0; u < 8; ++u) { const size_t n = (size_t)n0 + u;
;         ys[u] = *(const f32x4*)(c.w<float>(WS_YSSD) + n * 256 + t4); xr[u] = *(const uint2*)(c.w<bf16>(WS_XBCS) + n * 768 + t4); zr[u] = *(const uint2*)(c.w<bf16>(WS_Z) + n * 256 + t4); }
;     asm volatile("" ::: "memory");
; #pragma unroll
;     for (int u = 0; u < 8; ++u) {
;         const f32x4 x = bf4(xr[u]), z = bf4(zr[u]);
;         f32x4 y;
; #pragma unroll
;         for (int j = 0; j < 4; ++j) y[j] = (ys[u][j] + x[j] * dsk) * silu_f(z[j]);
.LBB0_301:
	s_mov_b64 s[0:1], -1
	s_cmpk_gt_i32 s51, 0x10f
	s_waitcnt vmcnt(0)
	v_bfe_u32 v72, v116, 4, 2
	s_cbranch_scc0 .LBB0_303
	s_load_dwordx4 s[16:19], s[4:5], 0xd0
	v_ashrrev_i32_e32 v2, 3, v116
	v_or_b32_e32 v6, s6, v72
	s_lshl_b64 s[0:1], s[46:47], 2
	v_and_b32_e32 v10, 63, v116
	v_and_b32_e32 v2, -8, v2
	s_waitcnt lgkmcnt(0)
	v_mov_b32_e32 v4, s16
	v_mov_b32_e32 v5, s17
	v_ashrrev_i32_e32 v7, 31, v6
	s_add_u32 s0, s18, s0
	v_add_u32_e32 v64, s50, v2
	v_lshl_add_u64 v[4:5], v[6:7], 2, v[4:5]
	s_addc_u32 s1, s19, s1
	v_lshlrev_b32_e32 v2, 4, v10
	global_load_dword v73, v[4:5], off
	s_mov_b64 s[16:17], 0xc546000
	global_load_dwordx4 v[4:7], v2, s[0:1]
	s_load_dwordx2 s[0:1], s[4:5], 0x130
	v_ashrrev_i32_e32 v65, 31, v64
	v_or_b32_e32 v44, 6, v64
	v_mov_b32_e32 v45, v65
	v_or_b32_e32 v74, 7, v64
	s_waitcnt lgkmcnt(0)
	v_lshl_add_u64 v[8:9], s[0:1], 0, v[2:3]
	v_lshlrev_b32_e32 v2, 3, v10
	v_lshl_add_u64 v[12:13], v[8:9], 0, s[16:17]
	v_lshl_add_u64 v[8:9], s[0:1], 0, v[2:3]
	s_mov_b64 s[16:17], 0xabc6000
	v_lshl_add_u64 v[10:11], v[8:9], 0, s[16:17]
	s_mov_b64 s[16:17], 0x67c6000
	v_lshl_add_u64 v[40:41], v[8:9], 0, s[16:17]
	v_lshlrev_b64 v[8:9], 10, v[64:65]
	v_lshl_add_u64 v[8:9], v[12:13], 0, v[8:9]
	global_load_dwordx4 v[32:35], v[8:9], off
	v_mad_i64_i32 v[8:9], s[16:17], v64, s39, v[10:11]
	v_lshlrev_b64 v[10:11], 9, v[64:65]
	v_lshl_add_u64 v[10:11], v[40:41], 0, v[10:11]
	global_load_dwordx2 v[66:67], v[8:9], off
	global_load_dwordx2 v[80:81], v[10:11], off
	global_load_dwordx2 v[68:69], v[8:9], off offset:1536
	global_load_dwordx2 v[62:63], v[8:9], off offset:3072
	v_or_b32_e32 v10, 1, v64
	v_mov_b32_e32 v11, v65
	v_lshlrev_b64 v[14:15], 10, v[10:11]
	v_lshlrev_b64 v[10:11], 9, v[10:11]
	v_lshl_add_u64 v[14:15], v[12:13], 0, v[14:15]
	v_lshl_add_u64 v[10:11], v[40:41], 0, v[10:11]
	global_load_dwordx4 v[36:39], v[14:15], off
	global_load_dwordx2 v[70:71], v[10:11], off
	s_mov_b64 s[16:17], 0x600
	v_lshl_add_u64 v[14:15], v[8:9], 0, s[16:17]
	v_or_b32_e32 v10, 2, v64
	v_mov_b32_e32 v11, v65
	s_mov_b64 s[16:17], 0xc00
	v_lshl_add_u64 v[20:21], v[8:9], 0, s[16:17]
	v_lshlrev_b64 v[8:9], 9, v[10:11]
	v_lshlrev_b64 v[16:17], 10, v[10:11]
	v_lshl_add_u64 v[8:9], v[40:41], 0, v[8:9]
	v_lshl_add_u64 v[16:17], v[12:13], 0, v[16:17]
	global_load_dwordx2 v[60:61], v[8:9], off
	global_load_dwordx2 v[58:59], v[14:15], off offset:3072
	global_load_dwordx4 v[24:27], v[16:17], off
	v_or_b32_e32 v8, 3, v64
	v_mov_b32_e32 v9, v65
	v_lshlrev_b64 v[10:11], 10, v[8:9]
	v_lshlrev_b64 v[8:9], 9, v[8:9]
	v_lshl_add_u64 v[10:11], v[12:13], 0, v[10:11]
	v_lshl_add_u64 v[8:9], v[40:41], 0, v[8:9]
	global_load_dwordx4 v[28:31], v[10:11], off
	global_load_dwordx2 v[56:57], v[8:9], off
	v_or_b32_e32 v8, 4, v64
	v_mov_b32_e32 v9, v65
	v_lshl_add_u64 v[10:11], v[14:15], 0, s[16:17]
	v_lshlrev_b64 v[14:15], 10, v[8:9]
	v_lshlrev_b64 v[8:9], 9, v[8:9]
	v_lshl_add_u64 v[8:9], v[40:41], 0, v[8:9]
	v_lshl_add_u64 v[14:15], v[12:13], 0, v[14:15]
	global_load_dwordx2 v[52:53], v[8:9], off
	global_load_dwordx2 v[50:51], v[10:11], off offset:3072
	v_or_b32_e32 v8, 5, v64
	v_mov_b32_e32 v9, v65
	global_load_dwordx4 v[16:19], v[14:15], off
	global_load_dwordx2 v[54:55], v[20:21], off offset:3072
	v_lshl_add_u64 v[14:15], v[20:21], 0, s[16:17]
	v_lshlrev_b64 v[20:21], 10, v[8:9]
	v_lshlrev_b64 v[8:9], 9, v[8:9]
	v_lshl_add_u64 v[20:21], v[12:13], 0, v[20:21]
	v_lshl_add_u64 v[8:9], v[40:41], 0, v[8:9]
	global_load_dwordx4 v[20:23], v[20:21], off
	v_lshl_add_u64 v[42:43], v[10:11], 0, s[16:17]
	global_load_dwordx2 v[48:49], v[8:9], off
	v_lshlrev_b64 v[8:9], 10, v[44:45]
	v_lshl_add_u64 v[8:9], v[12:13], 0, v[8:9]
	global_load_dwordx4 v[8:11], v[8:9], off
	s_nop 0
	global_load_dwordx2 v[46:47], v[14:15], off offset:3072
	v_lshlrev_b64 v[14:15], 9, v[44:45]
	v_lshl_add_u64 v[14:15], v[40:41], 0, v[14:15]
	v_mov_b32_e32 v75, v65
	global_load_dwordx2 v[44:45], v[14:15], off
	v_lshlrev_b64 v[14:15], 10, v[74:75]
	v_lshlrev_b64 v[74:75], 9, v[74:75]
	v_cmp_lt_i32_e32 vcc, v229, v228
	v_lshl_add_u64 v[40:41], v[40:41], 0, v[74:75]
	v_lshlrev_b64 v[64:65], 11, v[64:65]
	v_cndmask_b32_e32 v74, v222, v229, vcc
	v_lshlrev_b32_e32 v79, 2, v74
	v_cmp_lt_i32_e32 vcc, v230, v228
	v_lshl_add_u64 v[64:65], s[0:1], 0, v[64:65]
	s_mov_b32 s0, 0x358637bd
	v_cndmask_b32_e32 v74, v222, v230, vcc
	v_lshlrev_b32_e32 v78, 2, v74
	v_cmp_lt_i32_e32 vcc, v231, v228
	s_mov_b32 s16, 0x3b800000
	v_lshl_add_u64 v[12:13], v[12:13], 0, v[14:15]
	v_cndmask_b32_e32 v74, v222, v231, vcc
	v_lshlrev_b32_e32 v77, 2, v74
	v_cmp_lt_i32_e32 vcc, v232, v228
	global_load_dwordx4 v[12:15], v[12:13], off
	s_nop 0
	global_load_dwordx2 v[42:43], v[42:43], off offset:3072
	s_waitcnt vmcnt(21)
	v_lshlrev_b32_e32 v82, 16, v66
	v_and_b32_e32 v66, 0xffff0000, v66
	v_lshlrev_b32_e32 v83, 16, v67
	v_and_b32_e32 v84, 0xffff0000, v67
	s_waitcnt vmcnt(20)
	v_lshlrev_b32_e32 v67, 16, v80
	v_and_b32_e32 v80, 0xffff0000, v80
	v_fma_f32 v33, v73, v66, v33
	v_mul_f32_e32 v66, 0xbfb8aa3b, v80
	v_exp_f32_e32 v66, v66
	v_lshlrev_b32_e32 v85, 16, v81
	v_fma_f32 v32, v73, v82, v32
	v_mul_f32_e32 v82, 0xbfb8aa3b, v67
	v_add_f32_e32 v66, 1.0, v66
	v_rcp_f32_e32 v66, v66
	v_exp_f32_e32 v82, v82
	v_and_b32_e32 v81, 0xffff0000, v81
	v_fma_f32 v34, v73, v83, v34
	v_mul_f32_e32 v66, v66, v80
	v_mul_f32_e32 v33, v33, v66
	v_mul_f32_e32 v66, 0xbfb8aa3b, v85
	v_exp_f32_e32 v66, v66
	v_add_f32_e32 v82, 1.0, v82
	v_rcp_f32_e32 v82, v82
	s_waitcnt vmcnt(16)
; __device__ __forceinline__ float silu_f(float x) { return x * __builtin_amdgcn_rcpf(1.f + __expf(-x)); }
; __device__ __forceinline__ f32x4 bf4(const uint2 u) { return (f32x4){__uint_as_float(u.x << 16), __uint_as_float(u.x & 0xffff0000u), __uint_as_float(u.y << 16), __uint_as_float(u.y & 0xffff0000u)}; }
; __device__ __forceinline__ uint2 pack4(const f32x4 v) { uint2 o; o.x = pk2bf(v[0], v[1]); o.y = pk2bf(v[2], v[3]); return o; }
;     template <class T> __device__ __forceinline__ T* w(size_t off) const { return (T*)(p->ws + off); }
; __device__ __forceinline__ void ph_gates(const Ctx& c, int layer, int tile) {
;     ...
;     for (int u = 0; u < 8; ++u) {
;         const f32x4 x = bf4(xr[u]), z = bf4(zr[u]);
;         f32x4 y;
; #pragma unroll
;         for (int j = 0; j < 4; ++j) y[j] = (ys[u][j] + x[j] * dsk) * silu_f(z[j]);
;         const float ss = wave_sum(y[0] * y[0] + y[1] * y[1] + y[2] * y[2] + y[3] * y[3]);
;         const float rstd = rsqrtf(ss * (1.f / 256.f) + EPS);
;         *(uint2*)(c.w<bf16>(WS_MIX) + ((size_t)n0 + u) * D + 512 + t4) = pack4(y * rstd * gn);
	v_lshlrev_b32_e32 v80, 16, v70
	v_add_f32_e32 v66, 1.0, v66
	v_rcp_f32_e32 v66, v66
	v_mul_f32_e32 v67, v82, v67
	v_mul_f32_e32 v32, v32, v67
	v_and_b32_e32 v70, 0xffff0000, v70
	v_mul_f32_e32 v66, v66, v85
	v_mul_f32_e32 v67, v34, v66
	v_mul_f32_e32 v34, 0xbfb8aa3b, v81
	v_exp_f32_e32 v34, v34
	v_and_b32_e32 v66, 0xffff0000, v68
	v_lshlrev_b32_e32 v82, 16, v71
	v_and_b32_e32 v71, 0xffff0000, v71
	v_add_f32_e32 v34, 1.0, v34
	v_rcp_f32_e32 v34, v34
	v_fmac_f32_e32 v35, v73, v84
	v_mul_f32_e32 v83, v32, v32
	v_mul_f32_e32 v85, v33, v33
	v_mul_f32_e32 v81, v34, v81
	v_lshlrev_b32_e32 v34, 16, v68
	v_fma_f32 v34, v73, v34, v36
	v_mul_f32_e32 v36, 0xbfb8aa3b, v80
	v_exp_f32_e32 v36, v36
	v_lshlrev_b32_e32 v68, 16, v69
	v_and_b32_e32 v69, 0xffff0000, v69
	v_fmac_f32_e32 v39, v73, v69
	v_add_f32_e32 v36, 1.0, v36
	v_rcp_f32_e32 v36, v36
	v_cndmask_b32_e32 v74, v222, v232, vcc
	v_lshlrev_b32_e32 v76, 2, v74
	v_cmp_lt_i32_e32 vcc, v233, v228
	v_mul_f32_e32 v36, v36, v80
	v_mul_f32_e32 v36, v34, v36
	v_fma_f32 v34, v73, v66, v37
	v_mul_f32_e32 v37, 0xbfb8aa3b, v70
	v_exp_f32_e32 v37, v37
	v_cndmask_b32_e32 v74, v222, v233, vcc
	v_lshlrev_b32_e32 v75, 2, v74
	v_cmp_lt_i32_e32 vcc, v234, v228
	v_add_f32_e32 v37, 1.0, v37
	v_rcp_f32_e32 v37, v37
	v_cndmask_b32_e32 v74, v222, v234, vcc
	v_lshlrev_b32_e32 v74, 2, v74
	global_load_dwordx2 v[40:41], v[40:41], off
	v_mul_f32_e32 v37, v37, v70
	v_mul_f32_e32 v37, v34, v37
	v_fma_f32 v34, v73, v68, v38
	v_mul_f32_e32 v38, 0xbfb8aa3b, v82
	v_exp_f32_e32 v38, v38
	v_mul_f32_e32 v84, v37, v37
	v_add_f32_e32 v38, 1.0, v38
	v_rcp_f32_e32 v38, v38
	s_nop 0
	v_mul_f32_e32 v38, v38, v82
	v_mul_f32_e32 v66, v34, v38
	v_mul_f32_e32 v34, 0xbfb8aa3b, v71
	v_exp_f32_e32 v34, v34
	v_mul_f32_e32 v82, v36, v36
	v_add_f32_e32 v34, 1.0, v34
	v_rcp_f32_e32 v34, v34
	s_nop 0
	v_mul_f32_e32 v80, v34, v71
	v_mov_b32_e32 v34, v39
	v_pk_mul_f32 v[38:39], v[34:35], v[80:81]
	v_pk_add_f32 v[34:35], v[82:83], v[84:85]
	v_mov_b32_e32 v80, v67
	v_pk_fma_f32 v[34:35], v[66:67], v[66:67], v[34:35]
	v_mov_b32_e32 v81, v39
	v_pk_fma_f32 v[34:35], v[38:39], v[38:39], v[34:35]
	s_waitcnt lgkmcnt(0)
	v_mov_b32_e32 v67, v38
	s_nop 1
	v_add_f32_dpp v34, v34, v34 quad_perm:[1,0,3,2] row_mask:0xf bank_mask:0xf
	v_add_f32_dpp v35, v35, v35 quad_perm:[1,0,3,2] row_mask:0xf bank_mask:0xf
	s_nop 0
	v_add_f32_dpp v34, v34, v34 quad_perm:[2,3,0,1] row_mask:0xf bank_mask:0xf
	v_add_f32_dpp v35, v35, v35 quad_perm:[2,3,0,1] row_mask:0xf bank_mask:0xf
	s_nop 0
	v_add_f32_dpp v34, v34, v34 row_half_mirror row_mask:0xf bank_mask:0xf
	v_add_f32_dpp v35, v35, v35 row_half_mirror row_mask:0xf bank_mask:0xf
	s_nop 0
	v_add_f32_dpp v34, v34, v34 row_mirror row_mask:0xf bank_mask:0xf
	v_add_f32_dpp v35, v35, v35 row_mirror row_mask:0xf bank_mask:0xf
	s_nop 0
	v_mov_b32_e32 v68, v34
	v_mov_b32_e32 v69, v35
	s_nop 1
	v_permlane16_swap_b32_e32 v34, v68
	v_permlane16_swap_b32_e32 v35, v69
	v_pk_add_f32 v[34:35], v[34:35], v[68:69]
	v_mov_b32_e32 v68, v34
	v_mov_b32_e32 v69, v35
	s_nop 1
	v_permlane32_swap_b32_e32 v34, v68
	v_permlane32_swap_b32_e32 v35, v69
	v_pk_add_f32 v[68:69], v[34:35], v[68:69]
	v_mov_b64_e32 v[34:35], s[0:1]
	v_pk_fma_f32 v[68:69], v[68:69], s[16:17], v[34:35] op_sel_hi:[1,0,0]
	s_nop 0
	v_mul_f32_e32 v70, 0x4b800000, v69
	v_cmp_gt_f32_e64 s[0:1], s91, v69
	v_cmp_gt_f32_e32 vcc, s91, v68
	s_nop 0
	v_cndmask_b32_e64 v69, v69, v70, s[0:1]
	v_rsq_f32_e32 v69, v69
	s_nop 0
	v_mul_f32_e32 v70, 0x45800000, v69
	v_cndmask_b32_e64 v70, v69, v70, s[0:1]
	v_pk_mul_f32 v[32:33], v[32:33], v[70:71] op_sel_hi:[1,0]
	v_pk_mul_f32 v[70:71], v[80:81], v[70:71] op_sel_hi:[1,0]
	v_pk_mul_f32 v[32:33], v[4:5], v[32:33]
	s_mov_b32 s0, 0xdec6000
	v_cvt_pk_bf16_f32 v80, v32, v33
	v_lshl_add_u64 v[32:33], v[64:65], 0, v[2:3]
	v_mul_f32_e32 v2, 0x4b800000, v68
	v_cndmask_b32_e32 v2, v68, v2, vcc
	v_rsq_f32_e32 v2, v2
	v_add_co_u32_e64 v64, s[0:1], s0, v32
	v_pk_mul_f32 v[70:71], v[6:7], v[70:71]
	v_mul_f32_e32 v39, 0x45800000, v2
	v_cndmask_b32_e32 v2, v2, v39, vcc
	v_pk_mul_f32 v[36:37], v[36:37], v[2:3] op_sel_hi:[1,0]
	v_pk_mul_f32 v[38:39], v[66:67], v[2:3] op_sel_hi:[1,0]
	v_pk_mul_f32 v[36:37], v[4:5], v[36:37]
	v_pk_mul_f32 v[38:39], v[6:7], v[38:39]
	v_cvt_pk_bf16_f32 v36, v36, v37
	v_cvt_pk_bf16_f32 v37, v38, v39
	v_lshlrev_b32_e32 v2, 16, v62
	s_waitcnt vmcnt(16)
	v_lshlrev_b32_e32 v39, 16, v60
	s_waitcnt vmcnt(14)
	v_fma_f32 v2, v73, v2, v24
	v_mul_f32_e32 v24, 0xbfb8aa3b, v39
	v_exp_f32_e32 v24, v24
	v_addc_co_u32_e64 v65, s[0:1], 0, v33, s[0:1]
	global_store_dwordx2 v[64:65], v[36:37], off offset:3072
	v_add_f32_e32 v24, 1.0, v24
	v_rcp_f32_e32 v24, v24
	v_and_b32_e32 v36, 0xffff0000, v62
	v_and_b32_e32 v60, 0xffff0000, v60
	v_lshlrev_b32_e32 v37, 16, v63
	v_mul_f32_e32 v24, v24, v39
	v_mul_f32_e32 v24, v2, v24
	v_fma_f32 v2, v73, v36, v25
	v_mul_f32_e32 v25, 0xbfb8aa3b, v60
	v_exp_f32_e32 v25, v25
	v_lshlrev_b32_e32 v62, 16, v61
	v_and_b32_e32 v61, 0xffff0000, v61
	v_and_b32_e32 v38, 0xffff0000, v63
	v_add_f32_e32 v25, 1.0, v25
	v_rcp_f32_e32 v25, v25
	v_fmac_f32_e32 v27, v73, v38
	v_lshlrev_b32_e32 v36, 16, v59
	v_and_b32_e32 v38, 0xffff0000, v59
	v_mul_f32_e32 v25, v25, v60
	v_mul_f32_e32 v25, v2, v25
	v_fma_f32 v2, v73, v37, v26
	v_mul_f32_e32 v26, 0xbfb8aa3b, v62
	v_exp_f32_e32 v26, v26
	s_waitcnt vmcnt(13)
; __device__ __forceinline__ float silu_f(float x) { return x * __builtin_amdgcn_rcpf(1.f + __expf(-x)); }
; __device__ __forceinline__ f32x4 bf4(const uint2 u) { return (f32x4){__uint_as_float(u.x << 16), __uint_as_float(u.x & 0xffff0000u), __uint_as_float(u.y << 16), __uint_as_float(u.y & 0xffff0000u)}; }
; __device__ __forceinline__ uint2 pack4(const f32x4 v) { uint2 o; o.x = pk2bf(v[0], v[1]); o.y = pk2bf(v[2], v[3]); return o; }
;     template <class T> __device__ __forceinline__ T* w(size_t off) const { return (T*)(p->ws + off); }
; __device__ __forceinline__ void ph_gates(const Ctx& c, int layer, int tile) {
;     ...
;     for (int u = 0; u < 8; ++u) {
;         const f32x4 x = bf4(xr[u]), z = bf4(zr[u]);
;         f32x4 y;
; #pragma unroll
;         for (int j = 0; j < 4; ++j) y[j] = (ys[u][j] + x[j] * dsk) * silu_f(z[j]);
;         const float ss = wave_sum(y[0] * y[0] + y[1] * y[1] + y[2] * y[2] + y[3] * y[3]);
;         const float rstd = rsqrtf(ss * (1.f / 256.f) + EPS);
;         *(uint2*)(c.w<bf16>(WS_MIX) + ((size_t)n0 + u) * D + 512 + t4) = pack4(y * rstd * gn);
	v_lshlrev_b32_e32 v59, 16, v57
	v_and_b32_e32 v57, 0xffff0000, v57
	v_mul_f32_e32 v63, v25, v25
	v_add_f32_e32 v26, 1.0, v26
	v_rcp_f32_e32 v26, v26
	v_fmac_f32_e32 v31, v73, v38
	v_cvt_pk_bf16_f32 v81, v70, v71
	global_store_dwordx2 v[64:65], v[80:81], off offset:1024
	v_mul_f32_e32 v26, v26, v62
	v_mul_f32_e32 v37, v2, v26
	v_mul_f32_e32 v2, 0xbfb8aa3b, v61
	v_exp_f32_e32 v2, v2
	v_and_b32_e32 v26, 0xffff0000, v58
	v_add_f32_e32 v2, 1.0, v2
	v_rcp_f32_e32 v2, v2
	s_nop 0
	v_mul_f32_e32 v39, v2, v61
	v_lshlrev_b32_e32 v2, 16, v58
	v_lshlrev_b32_e32 v58, 16, v56
	v_fma_f32 v2, v73, v2, v28
	v_mul_f32_e32 v28, 0xbfb8aa3b, v58
	v_exp_f32_e32 v28, v28
	v_and_b32_e32 v56, 0xffff0000, v56
	v_mul_f32_e32 v61, v24, v24
	v_add_f32_e32 v28, 1.0, v28
	v_rcp_f32_e32 v28, v28
	s_nop 0
	v_mul_f32_e32 v28, v28, v58
	v_mul_f32_e32 v28, v2, v28
	v_fma_f32 v2, v73, v26, v29
	v_mul_f32_e32 v26, 0xbfb8aa3b, v56
	v_exp_f32_e32 v26, v26
	v_mul_f32_e32 v60, v28, v28
	v_add_f32_e32 v26, 1.0, v26
	v_rcp_f32_e32 v26, v26
	s_nop 0
	v_mul_f32_e32 v26, v26, v56
	v_mul_f32_e32 v29, v2, v26
	v_mul_f32_e32 v26, 0xbfb8aa3b, v59
	v_exp_f32_e32 v26, v26
	v_fma_f32 v2, v73, v36, v30
	v_mul_f32_e32 v62, v29, v29
	v_add_f32_e32 v26, 1.0, v26
	v_rcp_f32_e32 v26, v26
	s_nop 0
	v_mul_f32_e32 v26, v26, v59
	v_mul_f32_e32 v36, v2, v26
	v_mul_f32_e32 v2, 0xbfb8aa3b, v57
	v_exp_f32_e32 v2, v2
	v_mov_b32_e32 v26, v31
	v_pk_add_f32 v[30:31], v[60:61], v[62:63]
	v_add_f32_e32 v2, 1.0, v2
	v_rcp_f32_e32 v2, v2
	v_pk_fma_f32 v[30:31], v[36:37], v[36:37], v[30:31]
	v_mul_f32_e32 v38, v2, v57
	v_pk_mul_f32 v[26:27], v[26:27], v[38:39]
	s_nop 0
	v_pk_fma_f32 v[30:31], v[26:27], v[26:27], v[30:31]
	s_waitcnt lgkmcnt(0)
	s_nop 1
	v_add_f32_dpp v30, v30, v30 quad_perm:[1,0,3,2] row_mask:0xf bank_mask:0xf
	v_add_f32_dpp v31, v31, v31 quad_perm:[1,0,3,2] row_mask:0xf bank_mask:0xf
	s_nop 0
	v_add_f32_dpp v30, v30, v30 quad_perm:[2,3,0,1] row_mask:0xf bank_mask:0xf
	v_add_f32_dpp v31, v31, v31 quad_perm:[2,3,0,1] row_mask:0xf bank_mask:0xf
	s_nop 0
	v_add_f32_dpp v30, v30, v30 row_half_mirror row_mask:0xf bank_mask:0xf
	v_add_f32_dpp v31, v31, v31 row_half_mirror row_mask:0xf bank_mask:0xf
	s_nop 0
	v_add_f32_dpp v30, v30, v30 row_mirror row_mask:0xf bank_mask:0xf
	v_add_f32_dpp v31, v31, v31 row_mirror row_mask:0xf bank_mask:0xf
	s_nop 0
	v_mov_b32_e32 v38, v30
	v_mov_b32_e32 v39, v31
	s_nop 1
	v_permlane16_swap_b32_e32 v30, v38
	v_permlane16_swap_b32_e32 v31, v39
	v_pk_add_f32 v[30:31], v[30:31], v[38:39]
	v_mov_b32_e32 v38, v30
	v_mov_b32_e32 v39, v31
	s_nop 1
	v_permlane32_swap_b32_e32 v30, v38
	v_permlane32_swap_b32_e32 v31, v39
	v_pk_add_f32 v[30:31], v[30:31], v[38:39]
	s_nop 0
	v_pk_fma_f32 v[30:31], v[30:31], s[16:17], v[34:35] op_sel_hi:[1,0,0]
	v_mov_b32_e32 v38, v37
	v_mul_f32_e32 v2, 0x4b800000, v31
	v_cmp_gt_f32_e64 s[0:1], s91, v31
	v_mov_b32_e32 v39, v27
	v_cmp_gt_f32_e32 vcc, s91, v30
	v_cndmask_b32_e64 v2, v31, v2, s[0:1]
	v_rsq_f32_e32 v2, v2
	v_mov_b32_e32 v37, v26
	v_mul_f32_e32 v31, 0x45800000, v2
	v_cndmask_b32_e64 v2, v2, v31, s[0:1]
	v_pk_mul_f32 v[24:25], v[24:25], v[2:3] op_sel_hi:[1,0]
	v_pk_mul_f32 v[38:39], v[38:39], v[2:3] op_sel_hi:[1,0]
	v_mul_f32_e32 v2, 0x4b800000, v30
	v_cndmask_b32_e32 v2, v30, v2, vcc
	v_rsq_f32_e32 v2, v2
	v_pk_mul_f32 v[38:39], v[6:7], v[38:39]
	v_pk_mul_f32 v[24:25], v[4:5], v[24:25]
	s_mov_b32 s0, 0xdec7000
	v_cvt_pk_bf16_f32 v24, v24, v25
	v_cvt_pk_bf16_f32 v25, v38, v39
	v_add_co_u32_e64 v38, s[0:1], s0, v32
	s_waitcnt vmcnt(13)
	v_and_b32_e32 v30, 0xffff0000, v53
	v_addc_co_u32_e64 v39, s[0:1], 0, v33, s[0:1]
	global_store_dwordx2 v[38:39], v[24:25], off offset:1024
	v_mul_f32_e32 v24, 0x45800000, v2
	v_cndmask_b32_e32 v2, v2, v24, vcc
	v_pk_mul_f32 v[24:25], v[28:29], v[2:3] op_sel_hi:[1,0]
	v_pk_mul_f32 v[26:27], v[36:37], v[2:3] op_sel_hi:[1,0]
	v_pk_mul_f32 v[24:25], v[4:5], v[24:25]
	v_pk_mul_f32 v[26:27], v[6:7], v[26:27]
	v_cvt_pk_bf16_f32 v24, v24, v25
	v_cvt_pk_bf16_f32 v25, v26, v27
	s_waitcnt vmcnt(11)
	v_lshlrev_b32_e32 v2, 16, v54
	v_lshlrev_b32_e32 v27, 16, v52
	v_fma_f32 v2, v73, v2, v16
	v_mul_f32_e32 v16, 0xbfb8aa3b, v27
	v_exp_f32_e32 v16, v16
	global_store_dwordx2 v[38:39], v[24:25], off offset:3072
	v_and_b32_e32 v24, 0xffff0000, v54
	v_and_b32_e32 v28, 0xffff0000, v52
	v_add_f32_e32 v16, 1.0, v16
	v_rcp_f32_e32 v16, v16
	v_lshlrev_b32_e32 v25, 16, v55
	v_lshlrev_b32_e32 v29, 16, v53
	s_waitcnt vmcnt(10)
	v_lshlrev_b32_e32 v36, 16, v49
	v_mul_f32_e32 v16, v16, v27
	v_mul_f32_e32 v16, v2, v16
	v_fma_f32 v2, v73, v24, v17
	v_mul_f32_e32 v17, 0xbfb8aa3b, v28
	v_exp_f32_e32 v17, v17
	v_lshlrev_b32_e32 v24, 16, v51
	v_and_b32_e32 v37, 0xffff0000, v49
	v_and_b32_e32 v26, 0xffff0000, v55
	v_add_f32_e32 v17, 1.0, v17
	v_rcp_f32_e32 v17, v17
	v_fmac_f32_e32 v19, v73, v26
	v_and_b32_e32 v26, 0xffff0000, v51
	v_fmac_f32_e32 v23, v73, v26
	v_mul_f32_e32 v17, v17, v28
	v_mul_f32_e32 v17, v2, v17
	v_fma_f32 v2, v73, v25, v18
	v_mul_f32_e32 v18, 0xbfb8aa3b, v29
	v_exp_f32_e32 v18, v18
	v_lshlrev_b32_e32 v28, 16, v48
	v_mul_f32_e32 v31, v17, v17
	v_add_f32_e32 v18, 1.0, v18
	v_rcp_f32_e32 v18, v18
	s_nop 0
	v_mul_f32_e32 v18, v18, v29
	v_mul_f32_e32 v25, v2, v18
	v_mul_f32_e32 v2, 0xbfb8aa3b, v30
	v_exp_f32_e32 v2, v2
	v_and_b32_e32 v18, 0xffff0000, v50
	v_mul_f32_e32 v29, v16, v16
	v_add_f32_e32 v2, 1.0, v2
	v_rcp_f32_e32 v2, v2
	s_nop 0
	v_mul_f32_e32 v27, v2, v30
	v_lshlrev_b32_e32 v2, 16, v50
	v_fma_f32 v2, v73, v2, v20
	v_mul_f32_e32 v20, 0xbfb8aa3b, v28
	v_exp_f32_e32 v20, v20
	v_and_b32_e32 v30, 0xffff0000, v48
	v_add_f32_e32 v20, 1.0, v20
	v_rcp_f32_e32 v20, v20
	s_nop 0
	v_mul_f32_e32 v20, v20, v28
	v_mul_f32_e32 v20, v2, v20
	v_fma_f32 v2, v73, v18, v21
	v_mul_f32_e32 v18, 0xbfb8aa3b, v30
	v_exp_f32_e32 v18, v18
	v_mul_f32_e32 v28, v20, v20
	v_add_f32_e32 v18, 1.0, v18
	v_rcp_f32_e32 v18, v18
	s_nop 0
	v_mul_f32_e32 v18, v18, v30
	v_mul_f32_e32 v21, v2, v18
	v_mul_f32_e32 v18, 0xbfb8aa3b, v36
	v_exp_f32_e32 v18, v18
	v_fma_f32 v2, v73, v24, v22
	v_mul_f32_e32 v30, v21, v21
	v_add_f32_e32 v18, 1.0, v18
	v_rcp_f32_e32 v18, v18
	s_nop 0
	v_mul_f32_e32 v18, v18, v36
	v_mul_f32_e32 v24, v2, v18
	v_mul_f32_e32 v2, 0xbfb8aa3b, v37
	v_exp_f32_e32 v2, v2
	v_mov_b32_e32 v18, v23
	v_pk_add_f32 v[22:23], v[28:29], v[30:31]
	v_add_f32_e32 v2, 1.0, v2
	v_rcp_f32_e32 v2, v2
	v_pk_fma_f32 v[22:23], v[24:25], v[24:25], v[22:23]
	v_mul_f32_e32 v26, v2, v37
	v_pk_mul_f32 v[18:19], v[18:19], v[26:27]
	s_nop 0
	v_pk_fma_f32 v[22:23], v[18:19], v[18:19], v[22:23]
	s_waitcnt lgkmcnt(0)
; __device__ __forceinline__ float silu_f(float x) { return x * __builtin_amdgcn_rcpf(1.f + __expf(-x)); }
; __device__ __forceinline__ f32x4 bf4(const uint2 u) { return (f32x4){__uint_as_float(u.x << 16), __uint_as_float(u.x & 0xffff0000u), __uint_as_float(u.y << 16), __uint_as_float(u.y & 0xffff0000u)}; }
; __device__ __forceinline__ uint2 pack4(const f32x4 v) { uint2 o; o.x = pk2bf(v[0], v[1]); o.y = pk2bf(v[2], v[3]); return o; }
;     template <class T> __device__ __forceinline__ T* w(size_t off) const { return (T*)(p->ws + off); }
; __device__ __forceinline__ void ph_gates(const Ctx& c, int layer, int tile) {
;     ...
;     for (int u = 0; u < 8; ++u) {
;         const f32x4 x = bf4(xr[u]), z = bf4(zr[u]);
;         f32x4 y;
; #pragma unroll
;         for (int j = 0; j < 4; ++j) y[j] = (ys[u][j] + x[j] * dsk) * silu_f(z[j]);
;         const float ss = wave_sum(y[0] * y[0] + y[1] * y[1] + y[2] * y[2] + y[3] * y[3]);
;         const float rstd = rsqrtf(ss * (1.f / 256.f) + EPS);
;         *(uint2*)(c.w<bf16>(WS_MIX) + ((size_t)n0 + u) * D + 512 + t4) = pack4(y * rstd * gn);
	s_nop 1
	v_add_f32_dpp v22, v22, v22 quad_perm:[1,0,3,2] row_mask:0xf bank_mask:0xf
	v_add_f32_dpp v23, v23, v23 quad_perm:[1,0,3,2] row_mask:0xf bank_mask:0xf
	s_nop 0
	v_add_f32_dpp v22, v22, v22 quad_perm:[2,3,0,1] row_mask:0xf bank_mask:0xf
	v_add_f32_dpp v23, v23, v23 quad_perm:[2,3,0,1] row_mask:0xf bank_mask:0xf
	s_nop 0
	v_add_f32_dpp v22, v22, v22 row_half_mirror row_mask:0xf bank_mask:0xf
	v_add_f32_dpp v23, v23, v23 row_half_mirror row_mask:0xf bank_mask:0xf
	s_nop 0
	v_add_f32_dpp v22, v22, v22 row_mirror row_mask:0xf bank_mask:0xf
	v_add_f32_dpp v23, v23, v23 row_mirror row_mask:0xf bank_mask:0xf
	s_nop 0
	v_mov_b32_e32 v26, v22
	v_mov_b32_e32 v27, v23
	s_nop 1
	v_permlane16_swap_b32_e32 v22, v26
	v_permlane16_swap_b32_e32 v23, v27
	v_pk_add_f32 v[22:23], v[22:23], v[26:27]
	v_mov_b32_e32 v26, v22
	v_mov_b32_e32 v27, v23
	s_nop 1
	v_permlane32_swap_b32_e32 v22, v26
	v_permlane32_swap_b32_e32 v23, v27
	v_pk_add_f32 v[22:23], v[22:23], v[26:27]
	s_nop 0
	v_pk_fma_f32 v[22:23], v[22:23], s[16:17], v[34:35] op_sel_hi:[1,0,0]
	v_mov_b32_e32 v26, v25
	v_mul_f32_e32 v2, 0x4b800000, v23
	v_cmp_gt_f32_e64 s[0:1], s91, v23
	v_mov_b32_e32 v27, v19
	v_cmp_gt_f32_e32 vcc, s91, v22
	v_cndmask_b32_e64 v2, v23, v2, s[0:1]
	v_rsq_f32_e32 v2, v2
	v_mov_b32_e32 v25, v18
	v_mul_f32_e32 v23, 0x45800000, v2
	v_cndmask_b32_e64 v2, v2, v23, s[0:1]
	v_pk_mul_f32 v[16:17], v[16:17], v[2:3] op_sel_hi:[1,0]
	v_pk_mul_f32 v[26:27], v[26:27], v[2:3] op_sel_hi:[1,0]
	v_mul_f32_e32 v2, 0x4b800000, v22
	v_cndmask_b32_e32 v2, v22, v2, vcc
	v_rsq_f32_e32 v2, v2
	v_pk_mul_f32 v[26:27], v[6:7], v[26:27]
	v_pk_mul_f32 v[16:17], v[4:5], v[16:17]
	s_mov_b32 s0, 0xdec8000
	v_cvt_pk_bf16_f32 v16, v16, v17
	v_cvt_pk_bf16_f32 v17, v26, v27
	v_add_co_u32_e64 v26, s[0:1], s0, v32
	s_waitcnt vmcnt(7)
	v_and_b32_e32 v22, 0xffff0000, v45
	v_addc_co_u32_e64 v27, s[0:1], 0, v33, s[0:1]
	global_store_dwordx2 v[26:27], v[16:17], off offset:1024
	v_mul_f32_e32 v16, 0x45800000, v2
	v_cndmask_b32_e32 v2, v2, v16, vcc
	v_pk_mul_f32 v[16:17], v[20:21], v[2:3] op_sel_hi:[1,0]
	v_pk_mul_f32 v[18:19], v[24:25], v[2:3] op_sel_hi:[1,0]
	v_pk_mul_f32 v[16:17], v[4:5], v[16:17]
	v_pk_mul_f32 v[18:19], v[6:7], v[18:19]
	v_cvt_pk_bf16_f32 v16, v16, v17
	v_cvt_pk_bf16_f32 v17, v18, v19
	v_lshlrev_b32_e32 v2, 16, v46
	v_lshlrev_b32_e32 v19, 16, v44
	v_fma_f32 v2, v73, v2, v8
	v_mul_f32_e32 v8, 0xbfb8aa3b, v19
	v_exp_f32_e32 v8, v8
	global_store_dwordx2 v[26:27], v[16:17], off offset:3072
	v_and_b32_e32 v16, 0xffff0000, v46
	v_and_b32_e32 v20, 0xffff0000, v44
	v_add_f32_e32 v8, 1.0, v8
	v_rcp_f32_e32 v8, v8
	v_lshlrev_b32_e32 v17, 16, v47
	v_lshlrev_b32_e32 v21, 16, v45
	s_waitcnt vmcnt(6)
; __device__ __forceinline__ float silu_f(float x) { return x * __builtin_amdgcn_rcpf(1.f + __expf(-x)); }
; __device__ __forceinline__ f32x4 bf4(const uint2 u) { return (f32x4){__uint_as_float(u.x << 16), __uint_as_float(u.x & 0xffff0000u), __uint_as_float(u.y << 16), __uint_as_float(u.y & 0xffff0000u)}; }
; __device__ __forceinline__ uint2 pack4(const f32x4 v) { uint2 o; o.x = pk2bf(v[0], v[1]); o.y = pk2bf(v[2], v[3]); return o; }
;     template <class T> __device__ __forceinline__ T* w(size_t off) const { return (T*)(p->ws + off); }
; __device__ __forceinline__ void ph_gates(const Ctx& c, int layer, int tile) {
;     ...
;     for (int u = 0; u < 8; ++u) {
;         const f32x4 x = bf4(xr[u]), z = bf4(zr[u]);
;         f32x4 y;
; #pragma unroll
;         for (int j = 0; j < 4; ++j) y[j] = (ys[u][j] + x[j] * dsk) * silu_f(z[j]);
;         const float ss = wave_sum(y[0] * y[0] + y[1] * y[1] + y[2] * y[2] + y[3] * y[3]);
;         const float rstd = rsqrtf(ss * (1.f / 256.f) + EPS);
;         *(uint2*)(c.w<bf16>(WS_MIX) + ((size_t)n0 + u) * D + 512 + t4) = pack4(y * rstd * gn);
;     }
	v_lshlrev_b32_e32 v24, 16, v41
	v_mul_f32_e32 v8, v8, v19
	v_mul_f32_e32 v8, v2, v8
	v_fma_f32 v2, v73, v16, v9
	v_mul_f32_e32 v9, 0xbfb8aa3b, v20
	v_exp_f32_e32 v9, v9
	v_lshlrev_b32_e32 v16, 16, v43
	v_and_b32_e32 v25, 0xffff0000, v41
	v_and_b32_e32 v18, 0xffff0000, v47
	v_add_f32_e32 v9, 1.0, v9
	v_rcp_f32_e32 v9, v9
	v_fmac_f32_e32 v11, v73, v18
	v_and_b32_e32 v18, 0xffff0000, v43
	v_fmac_f32_e32 v15, v73, v18
	v_mul_f32_e32 v9, v9, v20
	v_mul_f32_e32 v9, v2, v9
	v_fma_f32 v2, v73, v17, v10
	v_mul_f32_e32 v10, 0xbfb8aa3b, v21
	v_exp_f32_e32 v10, v10
	v_lshlrev_b32_e32 v20, 16, v40
	v_mul_f32_e32 v23, v9, v9
	v_add_f32_e32 v10, 1.0, v10
	v_rcp_f32_e32 v10, v10
	s_nop 0
	v_mul_f32_e32 v10, v10, v21
	v_mul_f32_e32 v17, v2, v10
	v_mul_f32_e32 v2, 0xbfb8aa3b, v22
	v_exp_f32_e32 v2, v2
	v_and_b32_e32 v10, 0xffff0000, v42
	v_mul_f32_e32 v21, v8, v8
	v_add_f32_e32 v2, 1.0, v2
	v_rcp_f32_e32 v2, v2
	s_nop 0
	v_mul_f32_e32 v19, v2, v22
	v_lshlrev_b32_e32 v2, 16, v42
	v_fma_f32 v2, v73, v2, v12
	v_mul_f32_e32 v12, 0xbfb8aa3b, v20
	v_exp_f32_e32 v12, v12
	v_and_b32_e32 v22, 0xffff0000, v40
	v_add_f32_e32 v12, 1.0, v12
	v_rcp_f32_e32 v12, v12
	s_nop 0
	v_mul_f32_e32 v12, v12, v20
	v_mul_f32_e32 v12, v2, v12
	v_fma_f32 v2, v73, v10, v13
	v_mul_f32_e32 v10, 0xbfb8aa3b, v22
	v_exp_f32_e32 v10, v10
	v_mul_f32_e32 v20, v12, v12
	v_add_f32_e32 v10, 1.0, v10
	v_rcp_f32_e32 v10, v10
	s_nop 0
	v_mul_f32_e32 v10, v10, v22
	v_mul_f32_e32 v13, v2, v10
	v_mul_f32_e32 v10, 0xbfb8aa3b, v24
	v_exp_f32_e32 v10, v10
	v_fma_f32 v2, v73, v16, v14
	v_mul_f32_e32 v22, v13, v13
	v_add_f32_e32 v10, 1.0, v10
	v_rcp_f32_e32 v10, v10
	s_nop 0
	v_mul_f32_e32 v10, v10, v24
	v_mul_f32_e32 v16, v2, v10
	v_mul_f32_e32 v2, 0xbfb8aa3b, v25
	v_exp_f32_e32 v2, v2
	v_mov_b32_e32 v10, v15
	v_pk_add_f32 v[14:15], v[20:21], v[22:23]
	v_add_f32_e32 v2, 1.0, v2
	v_rcp_f32_e32 v2, v2
	v_pk_fma_f32 v[14:15], v[16:17], v[16:17], v[14:15]
	v_mul_f32_e32 v18, v2, v25
	v_pk_mul_f32 v[10:11], v[10:11], v[18:19]
	s_nop 0
	v_pk_fma_f32 v[14:15], v[10:11], v[10:11], v[14:15]
	s_waitcnt lgkmcnt(0)
	s_nop 1
	v_add_f32_dpp v14, v14, v14 quad_perm:[1,0,3,2] row_mask:0xf bank_mask:0xf
	v_add_f32_dpp v15, v15, v15 quad_perm:[1,0,3,2] row_mask:0xf bank_mask:0xf
	s_nop 0
	v_add_f32_dpp v14, v14, v14 quad_perm:[2,3,0,1] row_mask:0xf bank_mask:0xf
	v_add_f32_dpp v15, v15, v15 quad_perm:[2,3,0,1] row_mask:0xf bank_mask:0xf
	s_nop 0
	v_add_f32_dpp v14, v14, v14 row_half_mirror row_mask:0xf bank_mask:0xf
	v_add_f32_dpp v15, v15, v15 row_half_mirror row_mask:0xf bank_mask:0xf
	s_nop 0
	v_add_f32_dpp v14, v14, v14 row_mirror row_mask:0xf bank_mask:0xf
	v_add_f32_dpp v15, v15, v15 row_mirror row_mask:0xf bank_mask:0xf
	s_nop 0
	v_mov_b32_e32 v18, v14
	v_mov_b32_e32 v19, v15
	s_nop 1
	v_permlane16_swap_b32_e32 v14, v18
	v_permlane16_swap_b32_e32 v15, v19
	v_pk_add_f32 v[14:15], v[14:15], v[18:19]
	v_mov_b32_e32 v18, v14
	v_mov_b32_e32 v19, v15
	s_nop 1
	v_permlane32_swap_b32_e32 v14, v18
	v_permlane32_swap_b32_e32 v15, v19
	v_pk_add_f32 v[14:15], v[14:15], v[18:19]
	s_nop 0
	v_pk_fma_f32 v[14:15], v[14:15], s[16:17], v[34:35] op_sel_hi:[1,0,0]
	v_mov_b32_e32 v18, v17
	v_mul_f32_e32 v2, 0x4b800000, v15
	v_cmp_gt_f32_e64 s[0:1], s91, v15
	v_mov_b32_e32 v19, v11
	v_cmp_gt_f32_e32 vcc, s91, v14
	v_cndmask_b32_e64 v2, v15, v2, s[0:1]
	v_rsq_f32_e32 v2, v2
	v_mov_b32_e32 v17, v10
	v_mul_f32_e32 v15, 0x45800000, v2
	v_cndmask_b32_e64 v2, v2, v15, s[0:1]
	v_pk_mul_f32 v[8:9], v[8:9], v[2:3] op_sel_hi:[1,0]
	v_pk_mul_f32 v[18:19], v[18:19], v[2:3] op_sel_hi:[1,0]
	v_mul_f32_e32 v2, 0x4b800000, v14
	v_cndmask_b32_e32 v2, v14, v2, vcc
	v_rsq_f32_e32 v2, v2
	v_pk_mul_f32 v[18:19], v[6:7], v[18:19]
	v_pk_mul_f32 v[8:9], v[4:5], v[8:9]
	s_mov_b32 s0, 0xdec9000
	v_cvt_pk_bf16_f32 v8, v8, v9
	v_cvt_pk_bf16_f32 v9, v18, v19
	v_add_co_u32_e64 v18, s[0:1], s0, v32
	s_nop 1
	v_addc_co_u32_e64 v19, s[0:1], 0, v33, s[0:1]
	global_store_dwordx2 v[18:19], v[8:9], off offset:1024
	v_mul_f32_e32 v8, 0x45800000, v2
	v_cndmask_b32_e32 v2, v2, v8, vcc
	v_pk_mul_f32 v[8:9], v[12:13], v[2:3] op_sel_hi:[1,0]
	v_pk_mul_f32 v[10:11], v[16:17], v[2:3] op_sel_hi:[1,0]
	v_pk_mul_f32 v[4:5], v[4:5], v[8:9]
	s_mov_b64 s[0:1], 0xdec9c00
	v_cvt_pk_bf16_f32 v2, v4, v5
	v_pk_mul_f32 v[6:7], v[6:7], v[10:11]
	v_lshl_add_u64 v[4:5], v[32:33], 0, s[0:1]
	global_store_dword v[18:19], v2, off offset:3072
	s_mov_b64 s[0:1], 0

;     template <class T> __device__ __forceinline__ T* w(size_t off) const { return (T*)(p->ws + off); }
; __device__ __forceinline__ void ph_gates(const Ctx& c, int layer, int tile) {
;     const int lane = c.tid & 63, n0 = tile * 32 + (c.tid >> 6) * 8, t4 = lane * 4;
;     const float dsk = c.in(26)[layer * 4 + (lane >> 4)];
;     const f32x4 gn = *(const f32x4*)(c.in(27) + layer * 256 + t4);
;     f32x4 ys[8]; uint2 xr[8], zr[8];
; #pragma unroll
;     for (int u = 0; u < 8; ++u) { const size_t n = (size_t)n0 + u;
;         ys[u] = *(const f32x4*)(c.w<float>(WS_YSSD) + n * 256 + t4); xr[u] = *(const uint2*)(c.w<bf16>(WS_XBCS) + n * 768 + t4); zr[u] = *(const uint2*)(c.w<bf16>(WS_Z) + n * 256 + t4); }
;     asm volatile("" ::: "memory");
.LBB0_310:
	s_load_dwordx4 s[16:19], s[4:5], 0xd0
	v_ashrrev_i32_e32 v2, 3, v74
	v_and_b32_e32 v2, -8, v2
	v_add_u32_e32 v64, s28, v2
	v_bfe_u32 v2, v74, 4, 2
	v_or_b32_e32 v6, s6, v2
	v_and_b32_e32 v10, 63, v74
	s_waitcnt lgkmcnt(0)
	v_mov_b32_e32 v4, s16
	v_mov_b32_e32 v5, s17
	v_ashrrev_i32_e32 v7, 31, v6
	s_add_u32 s0, s18, s46
	v_lshl_add_u64 v[4:5], v[6:7], 2, v[4:5]
	s_addc_u32 s1, s19, s47
	v_lshlrev_b32_e32 v2, 4, v10
	global_load_dword v75, v[4:5], off
	v_ashrrev_i32_e32 v65, 31, v64
	global_load_dwordx4 v[4:7], v2, s[0:1]
	s_load_dwordx2 s[0:1], s[4:5], 0x130
	v_or_b32_e32 v44, 6, v64
	v_mov_b32_e32 v45, v65
	v_or_b32_e32 v76, 7, v64
	v_mov_b32_e32 v77, v65
	s_waitcnt lgkmcnt(0)
	v_lshl_add_u64 v[8:9], s[0:1], 0, v[2:3]
	v_lshlrev_b32_e32 v2, 3, v10
	v_lshl_add_u64 v[12:13], v[8:9], 0, s[44:45]
	v_lshl_add_u64 v[8:9], s[0:1], 0, v[2:3]
	v_lshl_add_u64 v[10:11], v[8:9], 0, s[48:49]
	v_lshl_add_u64 v[40:41], v[8:9], 0, s[42:43]
	v_lshlrev_b64 v[8:9], 10, v[64:65]
	v_lshl_add_u64 v[8:9], v[12:13], 0, v[8:9]
	global_load_dwordx4 v[32:35], v[8:9], off
	v_mad_i64_i32 v[8:9], s[16:17], v64, s39, v[10:11]
	v_lshlrev_b64 v[10:11], 9, v[64:65]
	v_lshl_add_u64 v[10:11], v[40:41], 0, v[10:11]
	global_load_dwordx2 v[66:67], v[10:11], off
	global_load_dwordx2 v[72:73], v[8:9], off
	global_load_dwordx2 v[70:71], v[8:9], off offset:1536
	global_load_dwordx2 v[62:63], v[8:9], off offset:3072
	v_or_b32_e32 v10, 1, v64
	v_mov_b32_e32 v11, v65
	v_lshlrev_b64 v[14:15], 10, v[10:11]
	v_lshlrev_b64 v[10:11], 9, v[10:11]
	v_lshl_add_u64 v[14:15], v[12:13], 0, v[14:15]
	v_lshl_add_u64 v[10:11], v[40:41], 0, v[10:11]
	global_load_dwordx4 v[36:39], v[14:15], off
	global_load_dwordx2 v[68:69], v[10:11], off
	v_or_b32_e32 v10, 2, v64
	v_mov_b32_e32 v11, v65
	v_lshl_add_u64 v[14:15], v[8:9], 0, s[50:51]
	v_lshl_add_u64 v[20:21], v[8:9], 0, s[56:57]
	v_lshlrev_b64 v[8:9], 9, v[10:11]
	v_lshlrev_b64 v[16:17], 10, v[10:11]
	v_lshl_add_u64 v[8:9], v[40:41], 0, v[8:9]
	v_lshl_add_u64 v[16:17], v[12:13], 0, v[16:17]
	global_load_dwordx2 v[60:61], v[8:9], off
	global_load_dwordx2 v[58:59], v[14:15], off offset:3072
	global_load_dwordx4 v[24:27], v[16:17], off
	v_or_b32_e32 v8, 3, v64
	v_mov_b32_e32 v9, v65
	v_lshlrev_b64 v[10:11], 10, v[8:9]
	v_lshlrev_b64 v[8:9], 9, v[8:9]
	v_lshl_add_u64 v[10:11], v[12:13], 0, v[10:11]
	v_lshl_add_u64 v[8:9], v[40:41], 0, v[8:9]
	global_load_dwordx4 v[28:31], v[10:11], off
	global_load_dwordx2 v[56:57], v[8:9], off
	v_or_b32_e32 v8, 4, v64
	v_mov_b32_e32 v9, v65
	v_lshl_add_u64 v[10:11], v[14:15], 0, s[56:57]
	v_lshlrev_b64 v[14:15], 10, v[8:9]
	v_lshlrev_b64 v[8:9], 9, v[8:9]
	v_lshl_add_u64 v[8:9], v[40:41], 0, v[8:9]
	v_lshl_add_u64 v[14:15], v[12:13], 0, v[14:15]
	global_load_dwordx2 v[52:53], v[8:9], off
	global_load_dwordx2 v[50:51], v[10:11], off offset:3072
	v_or_b32_e32 v8, 5, v64
	v_mov_b32_e32 v9, v65
	global_load_dwordx4 v[16:19], v[14:15], off
	global_load_dwordx2 v[54:55], v[20:21], off offset:3072
	v_lshl_add_u64 v[14:15], v[20:21], 0, s[56:57]
	v_lshlrev_b64 v[20:21], 10, v[8:9]
	v_lshlrev_b64 v[8:9], 9, v[8:9]
	v_lshl_add_u64 v[20:21], v[12:13], 0, v[20:21]
	v_lshl_add_u64 v[8:9], v[40:41], 0, v[8:9]
	global_load_dwordx4 v[20:23], v[20:21], off
	v_lshl_add_u64 v[42:43], v[10:11], 0, s[56:57]
	global_load_dwordx2 v[48:49], v[8:9], off
	v_lshlrev_b64 v[8:9], 10, v[44:45]
	v_lshl_add_u64 v[8:9], v[12:13], 0, v[8:9]
	global_load_dwordx4 v[8:11], v[8:9], off
	s_nop 0
	global_load_dwordx2 v[46:47], v[14:15], off offset:3072
	v_lshlrev_b64 v[14:15], 9, v[44:45]
	v_lshl_add_u64 v[14:15], v[40:41], 0, v[14:15]
	global_load_dwordx2 v[44:45], v[14:15], off
	v_lshlrev_b64 v[14:15], 10, v[76:77]
	v_lshlrev_b64 v[76:77], 9, v[76:77]
	v_cmp_lt_i32_e32 vcc, v229, v228
	v_lshl_add_u64 v[40:41], v[40:41], 0, v[76:77]
	v_lshlrev_b64 v[64:65], 11, v[64:65]
	v_cndmask_b32_e32 v76, v222, v229, vcc
	v_lshlrev_b32_e32 v76, 2, v76
	v_cmp_lt_i32_e32 vcc, v230, v228
	v_lshl_add_u64 v[64:65], s[0:1], 0, v[64:65]
	v_lshl_add_u64 v[12:13], v[12:13], 0, v[14:15]
	v_cndmask_b32_e32 v77, v222, v230, vcc
	v_lshlrev_b32_e32 v77, 2, v77
	v_cmp_lt_i32_e32 vcc, v231, v228
	global_load_dwordx4 v[12:15], v[12:13], off
	s_nop 0
	global_load_dwordx2 v[42:43], v[42:43], off offset:3072
	v_cndmask_b32_e32 v78, v222, v231, vcc
	v_lshlrev_b32_e32 v78, 2, v78
	v_cmp_lt_i32_e32 vcc, v232, v228
	global_load_dwordx2 v[40:41], v[40:41], off
	s_add_i32 s28, s28, s29
	v_cndmask_b32_e32 v79, v222, v232, vcc
	v_lshlrev_b32_e32 v79, 2, v79
	s_waitcnt vmcnt(22)
	v_lshlrev_b32_e32 v84, 16, v66
	v_and_b32_e32 v85, 0xffff0000, v66
	v_mul_f32_e32 v66, 0xbfb8aa3b, v84
	v_exp_f32_e32 v66, v66
	s_waitcnt vmcnt(21)
	v_lshlrev_b32_e32 v82, 16, v72
	v_and_b32_e32 v72, 0xffff0000, v72
	v_fma_f32 v32, v75, v82, v32
	v_add_f32_e32 v66, 1.0, v66
	v_rcp_f32_e32 v66, v66
	v_lshlrev_b32_e32 v86, 16, v67
	v_and_b32_e32 v87, 0xffff0000, v67
	v_lshlrev_b32_e32 v83, 16, v73
	v_mul_f32_e32 v66, v66, v84
	v_mul_f32_e32 v66, v32, v66
	v_fma_f32 v32, v75, v72, v33
	v_mul_f32_e32 v33, 0xbfb8aa3b, v85
	v_exp_f32_e32 v33, v33
	v_and_b32_e32 v73, 0xffff0000, v73
	v_fmac_f32_e32 v35, v75, v73
	s_waitcnt vmcnt(17)
; __device__ __forceinline__ float silu_f(float x) { return x * __builtin_amdgcn_rcpf(1.f + __expf(-x)); }
; __device__ __forceinline__ f32x4 bf4(const uint2 u) { return (f32x4){__uint_as_float(u.x << 16), __uint_as_float(u.x & 0xffff0000u), __uint_as_float(u.y << 16), __uint_as_float(u.y & 0xffff0000u)}; }
; __device__ __forceinline__ uint2 pack4(const f32x4 v) { uint2 o; o.x = pk2bf(v[0], v[1]); o.y = pk2bf(v[2], v[3]); return o; }
;     template <class T> __device__ __forceinline__ T* w(size_t off) const { return (T*)(p->ws + off); }
; __device__ __forceinline__ void ph_gates(const Ctx& c, int layer, int tile) {
;     ...
;     for (int u = 0; u < 8; ++u) {
;         const f32x4 x = bf4(xr[u]), z = bf4(zr[u]);
;         f32x4 y;
; #pragma unroll
;         for (int j = 0; j < 4; ++j) y[j] = (ys[u][j] + x[j] * dsk) * silu_f(z[j]);
;         const float ss = wave_sum(y[0] * y[0] + y[1] * y[1] + y[2] * y[2] + y[3] * y[3]);
;         const float rstd = rsqrtf(ss * (1.f / 256.f) + EPS);
;         *(uint2*)(c.w<bf16>(WS_MIX) + ((size_t)n0 + u) * D + 512 + t4) = pack4(y * rstd * gn);
	v_lshlrev_b32_e32 v72, 16, v68
	v_add_f32_e32 v33, 1.0, v33
	v_rcp_f32_e32 v33, v33
	v_and_b32_e32 v68, 0xffff0000, v68
	v_lshlrev_b32_e32 v82, 16, v69
	v_and_b32_e32 v69, 0xffff0000, v69
	v_mul_f32_e32 v33, v33, v85
	v_mul_f32_e32 v67, v32, v33
	v_mul_f32_e32 v33, 0xbfb8aa3b, v86
	v_exp_f32_e32 v33, v33
	v_fma_f32 v32, v75, v83, v34
	v_and_b32_e32 v34, 0xffff0000, v70
	v_mul_f32_e32 v83, v66, v66
	v_add_f32_e32 v33, 1.0, v33
	v_rcp_f32_e32 v33, v33
	v_mul_f32_e32 v85, v67, v67
	v_cmp_lt_i32_e32 vcc, v233, v228
	s_add_i32 s7, s7, s15
	v_mul_f32_e32 v33, v33, v86
	v_mul_f32_e32 v33, v32, v33
	v_mul_f32_e32 v32, 0xbfb8aa3b, v87
	v_exp_f32_e32 v32, v32
	v_cndmask_b32_e32 v80, v222, v233, vcc
	v_lshlrev_b32_e32 v80, 2, v80
	v_cmp_lt_i32_e32 vcc, v234, v228
	v_add_f32_e32 v32, 1.0, v32
	v_rcp_f32_e32 v32, v32
	v_cndmask_b32_e32 v81, v222, v234, vcc
	v_lshlrev_b32_e32 v81, 2, v81
	s_cmpk_gt_i32 s7, 0x21f
	v_mul_f32_e32 v73, v32, v87
	v_lshlrev_b32_e32 v32, 16, v70
	v_fma_f32 v32, v75, v32, v36
	v_mul_f32_e32 v36, 0xbfb8aa3b, v72
	v_exp_f32_e32 v36, v36
	v_lshlrev_b32_e32 v70, 16, v71
	v_and_b32_e32 v71, 0xffff0000, v71
	v_fmac_f32_e32 v39, v75, v71
	v_add_f32_e32 v36, 1.0, v36
	v_rcp_f32_e32 v36, v36
	s_nop 0
	v_mul_f32_e32 v36, v36, v72
	v_mul_f32_e32 v36, v32, v36
	v_fma_f32 v32, v75, v34, v37
	v_mul_f32_e32 v34, 0xbfb8aa3b, v68
	v_exp_f32_e32 v34, v34
	s_nop 0
	v_add_f32_e32 v34, 1.0, v34
	v_rcp_f32_e32 v34, v34
	s_nop 0
	v_mul_f32_e32 v34, v34, v68
	v_mul_f32_e32 v37, v32, v34
	v_mul_f32_e32 v34, 0xbfb8aa3b, v82
	v_exp_f32_e32 v34, v34
	v_fma_f32 v32, v75, v70, v38
	v_mul_f32_e32 v84, v37, v37
	v_add_f32_e32 v34, 1.0, v34
	v_rcp_f32_e32 v34, v34
	s_nop 0
	v_mul_f32_e32 v34, v34, v82
	v_mul_f32_e32 v32, v32, v34
	v_mul_f32_e32 v34, 0xbfb8aa3b, v69
	v_exp_f32_e32 v34, v34
	v_mul_f32_e32 v82, v36, v36
	v_add_f32_e32 v34, 1.0, v34
	v_rcp_f32_e32 v34, v34
	s_nop 0
	v_mul_f32_e32 v72, v34, v69
	v_mov_b32_e32 v34, v39
	v_pk_mul_f32 v[68:69], v[34:35], v[72:73]
	v_pk_add_f32 v[34:35], v[82:83], v[84:85]
	v_mov_b32_e32 v72, v33
	v_pk_fma_f32 v[34:35], v[32:33], v[32:33], v[34:35]
	v_mov_b32_e32 v73, v69
	v_pk_fma_f32 v[34:35], v[68:69], v[68:69], v[34:35]
	s_waitcnt lgkmcnt(0)
	s_nop 1
	v_add_f32_dpp v34, v34, v34 quad_perm:[1,0,3,2] row_mask:0xf bank_mask:0xf
	v_add_f32_dpp v35, v35, v35 quad_perm:[1,0,3,2] row_mask:0xf bank_mask:0xf
	s_nop 0
	v_add_f32_dpp v34, v34, v34 quad_perm:[2,3,0,1] row_mask:0xf bank_mask:0xf
	v_add_f32_dpp v35, v35, v35 quad_perm:[2,3,0,1] row_mask:0xf bank_mask:0xf
	s_nop 0
	v_add_f32_dpp v34, v34, v34 row_half_mirror row_mask:0xf bank_mask:0xf
	v_add_f32_dpp v35, v35, v35 row_half_mirror row_mask:0xf bank_mask:0xf
	s_nop 0
	v_add_f32_dpp v34, v34, v34 row_mirror row_mask:0xf bank_mask:0xf
	v_add_f32_dpp v35, v35, v35 row_mirror row_mask:0xf bank_mask:0xf
	s_nop 0
	v_mov_b32_e32 v38, v34
	v_mov_b32_e32 v39, v35
	s_nop 1
	v_permlane16_swap_b32_e32 v34, v38
	v_permlane16_swap_b32_e32 v35, v39
	v_pk_add_f32 v[34:35], v[34:35], v[38:39]
	v_mov_b32_e32 v38, v34
	v_mov_b32_e32 v39, v35
	s_nop 1
	v_permlane32_swap_b32_e32 v34, v38
	v_permlane32_swap_b32_e32 v35, v39
	v_pk_add_f32 v[38:39], v[34:35], v[38:39]
	v_mov_b64_e32 v[34:35], s[60:61]
	v_pk_fma_f32 v[70:71], v[38:39], s[58:59], v[34:35] op_sel_hi:[1,0,0]
	s_nop 0
	v_mul_f32_e32 v38, 0x4b800000, v71
	v_cmp_gt_f32_e64 s[0:1], s91, v71
	v_cmp_gt_f32_e32 vcc, s91, v70
	s_nop 0
	v_cndmask_b32_e64 v38, v71, v38, s[0:1]
	v_rsq_f32_e32 v38, v38
	s_nop 0
	v_mul_f32_e32 v39, 0x45800000, v38
	v_cndmask_b32_e64 v38, v38, v39, s[0:1]
	v_pk_mul_f32 v[66:67], v[66:67], v[38:39] op_sel_hi:[1,0]
	v_pk_mul_f32 v[38:39], v[72:73], v[38:39] op_sel_hi:[1,0]
	v_pk_mul_f32 v[66:67], v[4:5], v[66:67]
	v_pk_mul_f32 v[38:39], v[6:7], v[38:39]
	v_cvt_pk_bf16_f32 v66, v66, v67
	v_cvt_pk_bf16_f32 v67, v38, v39
	v_lshl_add_u64 v[38:39], v[64:65], 0, v[2:3]
	v_mul_f32_e32 v2, 0x4b800000, v70
	v_cndmask_b32_e32 v2, v70, v2, vcc
	v_rsq_f32_e32 v2, v2
	v_add_co_u32_e64 v64, s[0:1], s55, v38
	v_mul_f32_e32 v33, 0x45800000, v2
	v_cndmask_b32_e32 v2, v2, v33, vcc
	v_mov_b32_e32 v33, v68
	v_pk_mul_f32 v[36:37], v[36:37], v[2:3] op_sel_hi:[1,0]
	v_pk_mul_f32 v[32:33], v[32:33], v[2:3] op_sel_hi:[1,0]
	v_pk_mul_f32 v[36:37], v[4:5], v[36:37]
	v_pk_mul_f32 v[32:33], v[6:7], v[32:33]
	v_addc_co_u32_e64 v65, s[0:1], 0, v39, s[0:1]
	v_cvt_pk_bf16_f32 v36, v36, v37
	v_cvt_pk_bf16_f32 v37, v32, v33
	global_store_dwordx2 v[64:65], v[36:37], off offset:3072
	v_lshlrev_b32_e32 v2, 16, v62
	s_waitcnt vmcnt(17)
	v_lshlrev_b32_e32 v37, 16, v60
	s_waitcnt vmcnt(15)
	v_fma_f32 v2, v75, v2, v24
	v_mul_f32_e32 v24, 0xbfb8aa3b, v37
	v_exp_f32_e32 v24, v24
	v_and_b32_e32 v32, 0xffff0000, v62
	v_and_b32_e32 v60, 0xffff0000, v60
	v_lshlrev_b32_e32 v33, 16, v63
	v_add_f32_e32 v24, 1.0, v24
	v_rcp_f32_e32 v24, v24
	v_lshlrev_b32_e32 v62, 16, v61
	v_and_b32_e32 v61, 0xffff0000, v61
	v_and_b32_e32 v36, 0xffff0000, v63
	v_mul_f32_e32 v24, v24, v37
	v_mul_f32_e32 v24, v2, v24
	v_fma_f32 v2, v75, v32, v25
	v_mul_f32_e32 v25, 0xbfb8aa3b, v60
	v_exp_f32_e32 v25, v25
	v_fmac_f32_e32 v27, v75, v36
	v_lshlrev_b32_e32 v32, 16, v59
	v_and_b32_e32 v36, 0xffff0000, v59
	v_add_f32_e32 v25, 1.0, v25
	v_rcp_f32_e32 v25, v25
	s_waitcnt vmcnt(13)
; __device__ __forceinline__ float silu_f(float x) { return x * __builtin_amdgcn_rcpf(1.f + __expf(-x)); }
; __device__ __forceinline__ f32x4 bf4(const uint2 u) { return (f32x4){__uint_as_float(u.x << 16), __uint_as_float(u.x & 0xffff0000u), __uint_as_float(u.y << 16), __uint_as_float(u.y & 0xffff0000u)}; }
; __device__ __forceinline__ uint2 pack4(const f32x4 v) { uint2 o; o.x = pk2bf(v[0], v[1]); o.y = pk2bf(v[2], v[3]); return o; }
;     template <class T> __device__ __forceinline__ T* w(size_t off) const { return (T*)(p->ws + off); }
; __device__ __forceinline__ void ph_gates(const Ctx& c, int layer, int tile) {
;     ...
;     for (int u = 0; u < 8; ++u) {
;         const f32x4 x = bf4(xr[u]), z = bf4(zr[u]);
;         f32x4 y;
; #pragma unroll
;         for (int j = 0; j < 4; ++j) y[j] = (ys[u][j] + x[j] * dsk) * silu_f(z[j]);
;         const float ss = wave_sum(y[0] * y[0] + y[1] * y[1] + y[2] * y[2] + y[3] * y[3]);
;         const float rstd = rsqrtf(ss * (1.f / 256.f) + EPS);
;         *(uint2*)(c.w<bf16>(WS_MIX) + ((size_t)n0 + u) * D + 512 + t4) = pack4(y * rstd * gn);
	v_lshlrev_b32_e32 v59, 16, v57
	v_and_b32_e32 v57, 0xffff0000, v57
	v_fmac_f32_e32 v31, v75, v36
	v_mul_f32_e32 v25, v25, v60
	v_mul_f32_e32 v25, v2, v25
	v_fma_f32 v2, v75, v33, v26
	v_mul_f32_e32 v26, 0xbfb8aa3b, v62
	v_exp_f32_e32 v26, v26
	v_mul_f32_e32 v63, v25, v25
	global_store_dwordx2 v[64:65], v[66:67], off offset:1024
	v_add_f32_e32 v26, 1.0, v26
	v_rcp_f32_e32 v26, v26
	s_nop 0
	v_mul_f32_e32 v26, v26, v62
	v_mul_f32_e32 v33, v2, v26
	v_mul_f32_e32 v2, 0xbfb8aa3b, v61
	v_exp_f32_e32 v2, v2
	v_and_b32_e32 v26, 0xffff0000, v58
	v_add_f32_e32 v2, 1.0, v2
	v_rcp_f32_e32 v2, v2
	s_nop 0
	v_mul_f32_e32 v37, v2, v61
	v_lshlrev_b32_e32 v2, 16, v58
	v_lshlrev_b32_e32 v58, 16, v56
	v_fma_f32 v2, v75, v2, v28
	v_mul_f32_e32 v28, 0xbfb8aa3b, v58
	v_exp_f32_e32 v28, v28
	v_and_b32_e32 v56, 0xffff0000, v56
	v_mul_f32_e32 v61, v24, v24
	v_add_f32_e32 v28, 1.0, v28
	v_rcp_f32_e32 v28, v28
	s_nop 0
	v_mul_f32_e32 v28, v28, v58
	v_mul_f32_e32 v28, v2, v28
	v_fma_f32 v2, v75, v26, v29
	v_mul_f32_e32 v26, 0xbfb8aa3b, v56
	v_exp_f32_e32 v26, v26
	v_mul_f32_e32 v60, v28, v28
	v_add_f32_e32 v26, 1.0, v26
	v_rcp_f32_e32 v26, v26
	s_nop 0
	v_mul_f32_e32 v26, v26, v56
	v_mul_f32_e32 v29, v2, v26
	v_mul_f32_e32 v26, 0xbfb8aa3b, v59
	v_exp_f32_e32 v26, v26
	v_fma_f32 v2, v75, v32, v30
	v_mul_f32_e32 v62, v29, v29
	v_add_f32_e32 v26, 1.0, v26
	v_rcp_f32_e32 v26, v26
	s_nop 0
	v_mul_f32_e32 v26, v26, v59
	v_mul_f32_e32 v32, v2, v26
	v_mul_f32_e32 v2, 0xbfb8aa3b, v57
	v_exp_f32_e32 v2, v2
	v_mov_b32_e32 v26, v31
	v_pk_add_f32 v[30:31], v[60:61], v[62:63]
	v_add_f32_e32 v2, 1.0, v2
	v_rcp_f32_e32 v2, v2
	v_pk_fma_f32 v[30:31], v[32:33], v[32:33], v[30:31]
	v_mul_f32_e32 v36, v2, v57
	v_pk_mul_f32 v[26:27], v[26:27], v[36:37]
	s_nop 0
	v_pk_fma_f32 v[30:31], v[26:27], v[26:27], v[30:31]
	s_waitcnt lgkmcnt(0)
	s_nop 1
	v_add_f32_dpp v30, v30, v30 quad_perm:[1,0,3,2] row_mask:0xf bank_mask:0xf
	v_add_f32_dpp v31, v31, v31 quad_perm:[1,0,3,2] row_mask:0xf bank_mask:0xf
	s_nop 0
	v_add_f32_dpp v30, v30, v30 quad_perm:[2,3,0,1] row_mask:0xf bank_mask:0xf
	v_add_f32_dpp v31, v31, v31 quad_perm:[2,3,0,1] row_mask:0xf bank_mask:0xf
	s_nop 0
	v_add_f32_dpp v30, v30, v30 row_half_mirror row_mask:0xf bank_mask:0xf
	v_add_f32_dpp v31, v31, v31 row_half_mirror row_mask:0xf bank_mask:0xf
	s_nop 0
	v_add_f32_dpp v30, v30, v30 row_mirror row_mask:0xf bank_mask:0xf
	v_add_f32_dpp v31, v31, v31 row_mirror row_mask:0xf bank_mask:0xf
	s_nop 0
	v_mov_b32_e32 v36, v30
	v_mov_b32_e32 v37, v31
	s_nop 1
	v_permlane16_swap_b32_e32 v30, v36
	v_permlane16_swap_b32_e32 v31, v37
	v_pk_add_f32 v[30:31], v[30:31], v[36:37]
	v_mov_b32_e32 v36, v30
	v_mov_b32_e32 v37, v31
	s_nop 1
	v_permlane32_swap_b32_e32 v30, v36
	v_permlane32_swap_b32_e32 v31, v37
	v_pk_add_f32 v[30:31], v[30:31], v[36:37]
	s_nop 0
	v_pk_fma_f32 v[30:31], v[30:31], s[58:59], v[34:35] op_sel_hi:[1,0,0]
	v_mov_b32_e32 v36, v33
	v_mul_f32_e32 v2, 0x4b800000, v31
	v_cmp_gt_f32_e64 s[0:1], s91, v31
	v_mov_b32_e32 v37, v27
	v_cmp_gt_f32_e32 vcc, s91, v30
	v_cndmask_b32_e64 v2, v31, v2, s[0:1]
	v_rsq_f32_e32 v2, v2
	v_mov_b32_e32 v33, v26
	v_mul_f32_e32 v31, 0x45800000, v2
	v_cndmask_b32_e64 v2, v2, v31, s[0:1]
	v_pk_mul_f32 v[24:25], v[24:25], v[2:3] op_sel_hi:[1,0]
	v_pk_mul_f32 v[36:37], v[36:37], v[2:3] op_sel_hi:[1,0]
	v_mul_f32_e32 v2, 0x4b800000, v30
	v_cndmask_b32_e32 v2, v30, v2, vcc
	v_rsq_f32_e32 v2, v2
	v_pk_mul_f32 v[36:37], v[6:7], v[36:37]
	v_pk_mul_f32 v[24:25], v[4:5], v[24:25]
	s_waitcnt vmcnt(13)
	v_and_b32_e32 v30, 0xffff0000, v53
	v_cvt_pk_bf16_f32 v24, v24, v25
	v_cvt_pk_bf16_f32 v25, v36, v37
	v_add_co_u32_e64 v36, s[0:1], s59, v38
	s_nop 1
	v_addc_co_u32_e64 v37, s[0:1], 0, v39, s[0:1]
	global_store_dwordx2 v[36:37], v[24:25], off offset:1024
	v_mul_f32_e32 v24, 0x45800000, v2
	v_cndmask_b32_e32 v2, v2, v24, vcc
	v_pk_mul_f32 v[24:25], v[28:29], v[2:3] op_sel_hi:[1,0]
	v_pk_mul_f32 v[26:27], v[32:33], v[2:3] op_sel_hi:[1,0]
	v_pk_mul_f32 v[24:25], v[4:5], v[24:25]
	v_pk_mul_f32 v[26:27], v[6:7], v[26:27]
	v_cvt_pk_bf16_f32 v24, v24, v25
	v_cvt_pk_bf16_f32 v25, v26, v27
	s_waitcnt vmcnt(11)
	v_lshlrev_b32_e32 v2, 16, v54
	v_lshlrev_b32_e32 v27, 16, v52
	v_fma_f32 v2, v75, v2, v16
	v_mul_f32_e32 v16, 0xbfb8aa3b, v27
	v_exp_f32_e32 v16, v16
	global_store_dwordx2 v[36:37], v[24:25], off offset:3072
	v_and_b32_e32 v24, 0xffff0000, v54
	v_and_b32_e32 v28, 0xffff0000, v52
	v_add_f32_e32 v16, 1.0, v16
	v_rcp_f32_e32 v16, v16
	v_lshlrev_b32_e32 v25, 16, v55
	v_lshlrev_b32_e32 v29, 16, v53
	s_waitcnt vmcnt(10)
	v_lshlrev_b32_e32 v32, 16, v49
	v_mul_f32_e32 v16, v16, v27
	v_mul_f32_e32 v16, v2, v16
	v_fma_f32 v2, v75, v24, v17
	v_mul_f32_e32 v17, 0xbfb8aa3b, v28
	v_exp_f32_e32 v17, v17
	v_lshlrev_b32_e32 v24, 16, v51
	v_and_b32_e32 v33, 0xffff0000, v49
	v_and_b32_e32 v26, 0xffff0000, v55
	v_add_f32_e32 v17, 1.0, v17
	v_rcp_f32_e32 v17, v17
	v_fmac_f32_e32 v19, v75, v26
	v_and_b32_e32 v26, 0xffff0000, v51
	v_fmac_f32_e32 v23, v75, v26
	v_mul_f32_e32 v17, v17, v28
	v_mul_f32_e32 v17, v2, v17
	v_fma_f32 v2, v75, v25, v18
	v_mul_f32_e32 v18, 0xbfb8aa3b, v29
	v_exp_f32_e32 v18, v18
	v_lshlrev_b32_e32 v28, 16, v48
	v_mul_f32_e32 v31, v17, v17
	v_add_f32_e32 v18, 1.0, v18
	v_rcp_f32_e32 v18, v18
	s_nop 0
	v_mul_f32_e32 v18, v18, v29
	v_mul_f32_e32 v25, v2, v18
	v_mul_f32_e32 v2, 0xbfb8aa3b, v30
	v_exp_f32_e32 v2, v2
	v_and_b32_e32 v18, 0xffff0000, v50
	v_mul_f32_e32 v29, v16, v16
	v_add_f32_e32 v2, 1.0, v2
	v_rcp_f32_e32 v2, v2
	s_nop 0
	v_mul_f32_e32 v27, v2, v30
	v_lshlrev_b32_e32 v2, 16, v50
	v_fma_f32 v2, v75, v2, v20
	v_mul_f32_e32 v20, 0xbfb8aa3b, v28
	v_exp_f32_e32 v20, v20
	v_and_b32_e32 v30, 0xffff0000, v48
	v_add_f32_e32 v20, 1.0, v20
	v_rcp_f32_e32 v20, v20
	s_nop 0
	v_mul_f32_e32 v20, v20, v28
	v_mul_f32_e32 v20, v2, v20
	v_fma_f32 v2, v75, v18, v21
	v_mul_f32_e32 v18, 0xbfb8aa3b, v30
	v_exp_f32_e32 v18, v18
	v_mul_f32_e32 v28, v20, v20
	v_add_f32_e32 v18, 1.0, v18
	v_rcp_f32_e32 v18, v18
	s_nop 0
	v_mul_f32_e32 v18, v18, v30
	v_mul_f32_e32 v21, v2, v18
	v_mul_f32_e32 v18, 0xbfb8aa3b, v32
	v_exp_f32_e32 v18, v18
	v_fma_f32 v2, v75, v24, v22
	v_mul_f32_e32 v30, v21, v21
	v_add_f32_e32 v18, 1.0, v18
	v_rcp_f32_e32 v18, v18
	s_nop 0
	v_mul_f32_e32 v18, v18, v32
	v_mul_f32_e32 v24, v2, v18
	v_mul_f32_e32 v2, 0xbfb8aa3b, v33
	v_exp_f32_e32 v2, v2
	v_mov_b32_e32 v18, v23
	v_pk_add_f32 v[22:23], v[28:29], v[30:31]
	v_add_f32_e32 v2, 1.0, v2
	v_rcp_f32_e32 v2, v2
	v_pk_fma_f32 v[22:23], v[24:25], v[24:25], v[22:23]
	v_mul_f32_e32 v26, v2, v33
	v_pk_mul_f32 v[18:19], v[18:19], v[26:27]
	s_nop 0
	v_pk_fma_f32 v[22:23], v[18:19], v[18:19], v[22:23]
	s_waitcnt lgkmcnt(0)
; __device__ __forceinline__ float silu_f(float x) { return x * __builtin_amdgcn_rcpf(1.f + __expf(-x)); }
; __device__ __forceinline__ f32x4 bf4(const uint2 u) { return (f32x4){__uint_as_float(u.x << 16), __uint_as_float(u.x & 0xffff0000u), __uint_as_float(u.y << 16), __uint_as_float(u.y & 0xffff0000u)}; }
; __device__ __forceinline__ uint2 pack4(const f32x4 v) { uint2 o; o.x = pk2bf(v[0], v[1]); o.y = pk2bf(v[2], v[3]); return o; }
;     template <class T> __device__ __forceinline__ T* w(size_t off) const { return (T*)(p->ws + off); }
; __device__ __forceinline__ void ph_gates(const Ctx& c, int layer, int tile) {
;     ...
;     for (int u = 0; u < 8; ++u) {
;         const f32x4 x = bf4(xr[u]), z = bf4(zr[u]);
;         f32x4 y;
; #pragma unroll
;         for (int j = 0; j < 4; ++j) y[j] = (ys[u][j] + x[j] * dsk) * silu_f(z[j]);
;         const float ss = wave_sum(y[0] * y[0] + y[1] * y[1] + y[2] * y[2] + y[3] * y[3]);
;         const float rstd = rsqrtf(ss * (1.f / 256.f) + EPS);
;         *(uint2*)(c.w<bf16>(WS_MIX) + ((size_t)n0 + u) * D + 512 + t4) = pack4(y * rstd * gn);
; __global__ void __launch_bounds__(NTHR, 2) mk_fwd(Params prm) {
;     ...
;                         else for (int t = bid - 272; t < NT / 32; t += G - 272) { asm volatile("" : "+v"(c.tid)); ph_gates(c, layer, t); }
	s_nop 1
	v_add_f32_dpp v22, v22, v22 quad_perm:[1,0,3,2] row_mask:0xf bank_mask:0xf
	v_add_f32_dpp v23, v23, v23 quad_perm:[1,0,3,2] row_mask:0xf bank_mask:0xf
	s_nop 0
	v_add_f32_dpp v22, v22, v22 quad_perm:[2,3,0,1] row_mask:0xf bank_mask:0xf
	v_add_f32_dpp v23, v23, v23 quad_perm:[2,3,0,1] row_mask:0xf bank_mask:0xf
	s_nop 0
	v_add_f32_dpp v22, v22, v22 row_half_mirror row_mask:0xf bank_mask:0xf
	v_add_f32_dpp v23, v23, v23 row_half_mirror row_mask:0xf bank_mask:0xf
	s_nop 0
	v_add_f32_dpp v22, v22, v22 row_mirror row_mask:0xf bank_mask:0xf
	v_add_f32_dpp v23, v23, v23 row_mirror row_mask:0xf bank_mask:0xf
	s_nop 0
	v_mov_b32_e32 v26, v22
	v_mov_b32_e32 v27, v23
	s_nop 1
	v_permlane16_swap_b32_e32 v22, v26
	v_permlane16_swap_b32_e32 v23, v27
	v_pk_add_f32 v[22:23], v[22:23], v[26:27]
	v_mov_b32_e32 v26, v22
	v_mov_b32_e32 v27, v23
	s_nop 1
	v_permlane32_swap_b32_e32 v22, v26
	v_permlane32_swap_b32_e32 v23, v27
	v_pk_add_f32 v[22:23], v[22:23], v[26:27]
	s_nop 0
	v_pk_fma_f32 v[22:23], v[22:23], s[58:59], v[34:35] op_sel_hi:[1,0,0]
	v_mov_b32_e32 v26, v25
	v_mul_f32_e32 v2, 0x4b800000, v23
	v_cmp_gt_f32_e64 s[0:1], s91, v23
	v_mov_b32_e32 v27, v19
	v_cmp_gt_f32_e32 vcc, s91, v22
	v_cndmask_b32_e64 v2, v23, v2, s[0:1]
	v_rsq_f32_e32 v2, v2
	v_mov_b32_e32 v25, v18
	v_mul_f32_e32 v23, 0x45800000, v2
	v_cndmask_b32_e64 v2, v2, v23, s[0:1]
	v_pk_mul_f32 v[16:17], v[16:17], v[2:3] op_sel_hi:[1,0]
	v_pk_mul_f32 v[26:27], v[26:27], v[2:3] op_sel_hi:[1,0]
	v_mul_f32_e32 v2, 0x4b800000, v22
	v_cndmask_b32_e32 v2, v22, v2, vcc
	v_rsq_f32_e32 v2, v2
	v_pk_mul_f32 v[26:27], v[6:7], v[26:27]
	v_pk_mul_f32 v[16:17], v[4:5], v[16:17]
	s_waitcnt vmcnt(7)
	v_and_b32_e32 v22, 0xffff0000, v45
	v_cvt_pk_bf16_f32 v16, v16, v17
	v_cvt_pk_bf16_f32 v17, v26, v27
	v_add_co_u32_e64 v26, s[0:1], s61, v38
	s_nop 1
	v_addc_co_u32_e64 v27, s[0:1], 0, v39, s[0:1]
	global_store_dwordx2 v[26:27], v[16:17], off offset:1024
	v_mul_f32_e32 v16, 0x45800000, v2
	v_cndmask_b32_e32 v2, v2, v16, vcc
	v_pk_mul_f32 v[16:17], v[20:21], v[2:3] op_sel_hi:[1,0]
	v_pk_mul_f32 v[18:19], v[24:25], v[2:3] op_sel_hi:[1,0]
	v_pk_mul_f32 v[16:17], v[4:5], v[16:17]
	v_pk_mul_f32 v[18:19], v[6:7], v[18:19]
	v_cvt_pk_bf16_f32 v16, v16, v17
	v_cvt_pk_bf16_f32 v17, v18, v19
	v_lshlrev_b32_e32 v2, 16, v46
	v_lshlrev_b32_e32 v19, 16, v44
	v_fma_f32 v2, v75, v2, v8
	v_mul_f32_e32 v8, 0xbfb8aa3b, v19
	v_exp_f32_e32 v8, v8
	global_store_dwordx2 v[26:27], v[16:17], off offset:3072
	v_and_b32_e32 v16, 0xffff0000, v46
	v_and_b32_e32 v20, 0xffff0000, v44
	v_add_f32_e32 v8, 1.0, v8
	v_rcp_f32_e32 v8, v8
	v_lshlrev_b32_e32 v17, 16, v47
	v_lshlrev_b32_e32 v21, 16, v45
	s_waitcnt vmcnt(6)
	v_lshlrev_b32_e32 v24, 16, v41
	v_mul_f32_e32 v8, v8, v19
	v_mul_f32_e32 v8, v2, v8
	v_fma_f32 v2, v75, v16, v9
	v_mul_f32_e32 v9, 0xbfb8aa3b, v20
	v_exp_f32_e32 v9, v9
	v_lshlrev_b32_e32 v16, 16, v43
	v_and_b32_e32 v25, 0xffff0000, v41
	v_and_b32_e32 v18, 0xffff0000, v47
	v_add_f32_e32 v9, 1.0, v9
	v_rcp_f32_e32 v9, v9
	v_fmac_f32_e32 v11, v75, v18
	v_and_b32_e32 v18, 0xffff0000, v43
	v_fmac_f32_e32 v15, v75, v18
	v_mul_f32_e32 v9, v9, v20
	v_mul_f32_e32 v9, v2, v9
	v_fma_f32 v2, v75, v17, v10
	v_mul_f32_e32 v10, 0xbfb8aa3b, v21
	v_exp_f32_e32 v10, v10
	v_lshlrev_b32_e32 v20, 16, v40
	v_mul_f32_e32 v23, v9, v9
	v_add_f32_e32 v10, 1.0, v10
	v_rcp_f32_e32 v10, v10
	s_nop 0
	v_mul_f32_e32 v10, v10, v21
	v_mul_f32_e32 v17, v2, v10
	v_mul_f32_e32 v2, 0xbfb8aa3b, v22
	v_exp_f32_e32 v2, v2
	v_and_b32_e32 v10, 0xffff0000, v42
	v_mul_f32_e32 v21, v8, v8
	v_add_f32_e32 v2, 1.0, v2
	v_rcp_f32_e32 v2, v2
	s_nop 0
	v_mul_f32_e32 v19, v2, v22
	v_lshlrev_b32_e32 v2, 16, v42
	v_fma_f32 v2, v75, v2, v12
	v_mul_f32_e32 v12, 0xbfb8aa3b, v20
	v_exp_f32_e32 v12, v12
	v_and_b32_e32 v22, 0xffff0000, v40
	v_add_f32_e32 v12, 1.0, v12
	v_rcp_f32_e32 v12, v12
	s_nop 0
	v_mul_f32_e32 v12, v12, v20
	v_mul_f32_e32 v12, v2, v12
	v_fma_f32 v2, v75, v10, v13
	v_mul_f32_e32 v10, 0xbfb8aa3b, v22
	v_exp_f32_e32 v10, v10
	v_mul_f32_e32 v20, v12, v12
	v_add_f32_e32 v10, 1.0, v10
	v_rcp_f32_e32 v10, v10
	s_nop 0
	v_mul_f32_e32 v10, v10, v22
	v_mul_f32_e32 v13, v2, v10
	v_mul_f32_e32 v10, 0xbfb8aa3b, v24
	v_exp_f32_e32 v10, v10
	v_fma_f32 v2, v75, v16, v14
	v_mul_f32_e32 v22, v13, v13
	v_add_f32_e32 v10, 1.0, v10
	v_rcp_f32_e32 v10, v10
	s_nop 0
	v_mul_f32_e32 v10, v10, v24
	v_mul_f32_e32 v16, v2, v10
	v_mul_f32_e32 v2, 0xbfb8aa3b, v25
	v_exp_f32_e32 v2, v2
	v_mov_b32_e32 v10, v15
	v_pk_add_f32 v[14:15], v[20:21], v[22:23]
	v_add_f32_e32 v2, 1.0, v2
	v_rcp_f32_e32 v2, v2
	v_pk_fma_f32 v[14:15], v[16:17], v[16:17], v[14:15]
	v_mul_f32_e32 v18, v2, v25
	v_pk_mul_f32 v[10:11], v[10:11], v[18:19]
	s_nop 0
	v_pk_fma_f32 v[14:15], v[10:11], v[10:11], v[14:15]
	s_waitcnt lgkmcnt(0)
	s_nop 1
	v_add_f32_dpp v14, v14, v14 quad_perm:[1,0,3,2] row_mask:0xf bank_mask:0xf
	v_add_f32_dpp v15, v15, v15 quad_perm:[1,0,3,2] row_mask:0xf bank_mask:0xf
	s_nop 0
	v_add_f32_dpp v14, v14, v14 quad_perm:[2,3,0,1] row_mask:0xf bank_mask:0xf
	v_add_f32_dpp v15, v15, v15 quad_perm:[2,3,0,1] row_mask:0xf bank_mask:0xf
	s_nop 0
	v_add_f32_dpp v14, v14, v14 row_half_mirror row_mask:0xf bank_mask:0xf
	v_add_f32_dpp v15, v15, v15 row_half_mirror row_mask:0xf bank_mask:0xf
	s_nop 0
	v_add_f32_dpp v14, v14, v14 row_mirror row_mask:0xf bank_mask:0xf
	v_add_f32_dpp v15, v15, v15 row_mirror row_mask:0xf bank_mask:0xf
	s_nop 0
	v_mov_b32_e32 v18, v14
	v_mov_b32_e32 v19, v15
	s_nop 1
	v_permlane16_swap_b32_e32 v14, v18
	v_permlane16_swap_b32_e32 v15, v19
	v_pk_add_f32 v[14:15], v[14:15], v[18:19]
	v_mov_b32_e32 v18, v14
	v_mov_b32_e32 v19, v15
	s_nop 1
	v_permlane32_swap_b32_e32 v14, v18
	v_permlane32_swap_b32_e32 v15, v19
	v_pk_add_f32 v[14:15], v[14:15], v[18:19]
	s_nop 0
	v_pk_fma_f32 v[14:15], v[14:15], s[58:59], v[34:35] op_sel_hi:[1,0,0]
	v_mov_b32_e32 v18, v17
	v_mul_f32_e32 v2, 0x4b800000, v15
	v_cmp_gt_f32_e64 s[0:1], s91, v15
	v_mov_b32_e32 v19, v11
	v_cmp_gt_f32_e32 vcc, s91, v14
	v_cndmask_b32_e64 v2, v15, v2, s[0:1]
	v_rsq_f32_e32 v2, v2
	v_mov_b32_e32 v17, v10
	v_mul_f32_e32 v15, 0x45800000, v2
	v_cndmask_b32_e64 v2, v2, v15, s[0:1]
	v_pk_mul_f32 v[8:9], v[8:9], v[2:3] op_sel_hi:[1,0]
	v_pk_mul_f32 v[18:19], v[18:19], v[2:3] op_sel_hi:[1,0]
	v_mul_f32_e32 v2, 0x4b800000, v14
	v_cndmask_b32_e32 v2, v14, v2, vcc
	v_rsq_f32_e32 v2, v2
	v_pk_mul_f32 v[18:19], v[6:7], v[18:19]
	v_pk_mul_f32 v[8:9], v[4:5], v[8:9]
	s_nop 0
	v_cvt_pk_bf16_f32 v8, v8, v9
	v_cvt_pk_bf16_f32 v9, v18, v19
	v_add_co_u32_e64 v18, s[0:1], s62, v38
	s_nop 1
	v_addc_co_u32_e64 v19, s[0:1], 0, v39, s[0:1]
	global_store_dwordx2 v[18:19], v[8:9], off offset:1024
	v_mul_f32_e32 v8, 0x45800000, v2
	v_cndmask_b32_e32 v2, v2, v8, vcc
	v_pk_mul_f32 v[8:9], v[12:13], v[2:3] op_sel_hi:[1,0]
	v_pk_mul_f32 v[10:11], v[16:17], v[2:3] op_sel_hi:[1,0]
	v_pk_mul_f32 v[4:5], v[4:5], v[8:9]
	v_pk_mul_f32 v[6:7], v[6:7], v[10:11]
	v_cvt_pk_bf16_f32 v4, v4, v5
	v_cvt_pk_bf16_f32 v5, v6, v7
	global_store_dwordx2 v[18:19], v[4:5], off offset:3072
	s_cbranch_scc0 .LBB0_310
